# v14 + top-k phase: waves 4-7 start their item loop ~3.4 us later (one s_sleep) so the two waves of a SIMD are out of phase and their load stalls no longer coincide
# speedup vs baseline: 1.0025x; 1.0014x over previous
; #define GAS __attribute__((address_space(1)))
; #define LAS __attribute__((address_space(3)))
; DI unsigned pk2(float lo, float hi) { return f2bf(lo) | (f2bf(hi) << 16); }
; DI void p8_phase(Frame& F) {
;     LAS unsigned char* KIMG = F.lds; LAS unsigned char* TBL = F.lds + P8_TBL + F.wave * 1024;
;     const int lane = F.lane, tid = F.tid, r = lane & 31, h = lane >> 5;
; #pragma unroll 4
;     for (int i = 0; i < 16; ++i) { const int idx = tid * 4 + 2048 * i, side = idx >> 14, rem = idx & 16383, row = rem >> 7, col = rem & 127;
;         const f32x4 a = *(const GAS f32x4*)((side ? F.keys2 : F.keys1) + rem);
;         v2u o; o.x = pk2(a.x, a.y); o.y = pk2(a.z, a.w); *(LAS v2u*)(KIMG + (side * 128 + row) * KPITCH + col * 2) = o; }
.LBB0_1201:
	v_readlane_b32 s4, v252, 4
	v_readlane_b32 s5, v252, 5
	s_cmp_lt_i32 s4, 9
	v_readlane_b32 s4, v252, 13
	s_cselect_b64 s[2:3], -1, 0
	v_readlane_b32 s5, v252, 14
	s_add_u32 s14, s4, 0x3400000
	s_addc_u32 s15, s5, 0
	s_add_u32 s16, s4, 0x2c00000
	s_addc_u32 s17, s5, 0
	s_add_u32 s37, s4, 0x18000000
	s_addc_u32 s39, s5, 0
	s_add_u32 s18, s4, 0x1a000000
	s_addc_u32 s19, s5, 0
	s_add_u32 s20, s4, 0x380000
	s_addc_u32 s21, s5, 0
	s_add_u32 s24, s4, 0x390000
	s_addc_u32 s25, s5, 0
	s_and_b64 s[8:9], s[2:3], s[0:1]
	s_andn2_b64 vcc, exec, s[8:9]
	v_readlane_b32 s6, v252, 6
	v_readlane_b32 s7, v252, 7
	s_cbranch_vccnz .LBB0_1246
	v_lshlrev_b32_e32 v1, 3, v0
	v_lshrrev_b32_e32 v3, 5, v0
	s_waitcnt lgkmcnt(0)
	v_and_b32_e32 v2, 0xf8, v1
	v_or_b32_e32 v1, 48, v3
	v_or_b32_e32 v4, 32, v3
	v_or_b32_e32 v5, 16, v3
	v_mul_u32_u24_e32 v1, 0x110, v1
	v_mul_u32_u24_e32 v4, 0x110, v4
	v_mul_u32_u24_e32 v5, 0x110, v5
	v_mul_u32_u24_e32 v3, 0x110, v3
	s_mov_b32 s2, 0
	v_add3_u32 v1, v1, v2, 0
	v_add3_u32 v4, v4, v2, 0
	v_add3_u32 v5, v5, v2, 0
	v_add3_u32 v6, v3, v2, 0
	s_movk_i32 s3, 0x7fff
	s_mov_b32 s4, 0xffff0000
	s_movk_i32 s5, 0x4000
	v_mov_b32_e32 v7, s79
	s_waitcnt vmcnt(31)
	v_mov_b32_e32 v8, s77
	s_waitcnt vmcnt(30)
	v_mov_b32_e32 v9, s78
	v_mov_b32_e32 v10, s76
	v_mov_b32_e32 v3, 0
	s_mov_b32 s6, 0
	v_add_u32_e32 v2, s2, v150
	s_cmp_lt_u32 s6, 8
	v_and_b32_e32 v11, 0x2ffc, v2
	v_add_u32_e32 v40, 0x800, v2
	v_add_u32_e32 v41, 0x1000, v2
	s_cselect_b32 s11, s77, s79
	s_cselect_b32 s10, s76, s78
	s_cmpk_lt_u32 s2, 0x4000
	v_add_u32_e32 v2, 0x1800, v2
	v_lshlrev_b32_e32 v11, 2, v11
	v_and_b32_e32 v44, 0x3ffc, v40
	v_cmp_gt_u32_e32 vcc, s5, v40
	v_and_b32_e32 v45, 0x3ffc, v41
	s_cselect_b32 s13, s77, s79
	v_cndmask_b32_e32 v49, v7, v8, vcc
	s_cselect_b32 s12, s76, s78
	v_and_b32_e32 v50, 0x3ffc, v2
	v_cmp_gt_u32_e64 s[0:1], s5, v2
	global_load_dwordx4 v[40:43], v11, s[10:11]
	v_cndmask_b32_e32 v48, v9, v10, vcc
	v_lshlrev_b32_e32 v2, 2, v44
	v_lshlrev_b32_e32 v11, 2, v45
	v_cndmask_b32_e64 v53, v7, v8, s[0:1]
	v_cndmask_b32_e64 v52, v9, v10, s[0:1]
	global_load_dwordx4 v[44:47], v11, s[12:13]
	v_lshl_add_u64 v[48:49], v[48:49], 0, v[2:3]
	v_lshlrev_b32_e32 v2, 2, v50
	global_load_dwordx4 v[48:51], v[48:49], off
	v_lshl_add_u64 v[52:53], v[52:53], 0, v[2:3]
	global_load_dwordx4 v[52:55], v[52:53], off
	s_add_i32 s6, s6, 4
	s_addk_i32 s2, 0x2000
	s_cmpk_eq_u32 s2, 0x8000
	v_add_u32_e32 v2, s2, v150
	s_cmp_lt_u32 s6, 8
	v_and_b32_e32 v11, 0x2ffc, v2
	v_add_u32_e32 v56, 0x800, v2
	v_add_u32_e32 v57, 0x1000, v2
	s_cselect_b32 s11, s77, s79
	s_cselect_b32 s10, s76, s78
	s_cmpk_lt_u32 s2, 0x4000
	v_add_u32_e32 v2, 0x1800, v2
	v_lshlrev_b32_e32 v11, 2, v11
	v_and_b32_e32 v60, 0x3ffc, v56
	v_cmp_gt_u32_e32 vcc, s5, v56
	v_and_b32_e32 v61, 0x3ffc, v57
	s_cselect_b32 s13, s77, s79
	v_cndmask_b32_e32 v65, v7, v8, vcc
	s_cselect_b32 s12, s76, s78
	v_and_b32_e32 v66, 0x3ffc, v2
	v_cmp_gt_u32_e64 s[0:1], s5, v2
	global_load_dwordx4 v[56:59], v11, s[10:11]
	v_cndmask_b32_e32 v64, v9, v10, vcc
	v_lshlrev_b32_e32 v2, 2, v60
	v_lshlrev_b32_e32 v11, 2, v61
	v_cndmask_b32_e64 v69, v7, v8, s[0:1]
	v_cndmask_b32_e64 v68, v9, v10, s[0:1]
	global_load_dwordx4 v[60:63], v11, s[12:13]
	v_lshl_add_u64 v[64:65], v[64:65], 0, v[2:3]
	v_lshlrev_b32_e32 v2, 2, v66
	global_load_dwordx4 v[64:67], v[64:65], off
	v_lshl_add_u64 v[68:69], v[68:69], 0, v[2:3]
	global_load_dwordx4 v[68:71], v[68:69], off
	s_add_i32 s6, s6, 4
	s_addk_i32 s2, 0x2000
	s_cmpk_eq_u32 s2, 0x8000
	v_add_u32_e32 v2, s2, v150
	s_cmp_lt_u32 s6, 8
	v_and_b32_e32 v11, 0x2ffc, v2
	v_add_u32_e32 v72, 0x800, v2
	v_add_u32_e32 v73, 0x1000, v2
	s_cselect_b32 s11, s77, s79
	s_cselect_b32 s10, s76, s78
	s_cmpk_lt_u32 s2, 0x4000
	v_add_u32_e32 v2, 0x1800, v2
	v_lshlrev_b32_e32 v11, 2, v11
	v_and_b32_e32 v76, 0x3ffc, v72
	v_cmp_gt_u32_e32 vcc, s5, v72
	v_and_b32_e32 v77, 0x3ffc, v73
	s_cselect_b32 s13, s77, s79
	v_cndmask_b32_e32 v81, v7, v8, vcc
	s_cselect_b32 s12, s76, s78
	v_and_b32_e32 v82, 0x3ffc, v2
	v_cmp_gt_u32_e64 s[0:1], s5, v2
	global_load_dwordx4 v[72:75], v11, s[10:11]
	v_cndmask_b32_e32 v80, v9, v10, vcc
	v_lshlrev_b32_e32 v2, 2, v76
	v_lshlrev_b32_e32 v11, 2, v77
	v_cndmask_b32_e64 v85, v7, v8, s[0:1]
	v_cndmask_b32_e64 v84, v9, v10, s[0:1]
	global_load_dwordx4 v[76:79], v11, s[12:13]
	v_lshl_add_u64 v[80:81], v[80:81], 0, v[2:3]
	v_lshlrev_b32_e32 v2, 2, v82
	global_load_dwordx4 v[80:83], v[80:81], off
	v_lshl_add_u64 v[84:85], v[84:85], 0, v[2:3]
	global_load_dwordx4 v[84:87], v[84:85], off
	s_add_i32 s6, s6, 4
	s_addk_i32 s2, 0x2000
	s_cmpk_eq_u32 s2, 0x8000
	v_add_u32_e32 v2, s2, v150
	s_cmp_lt_u32 s6, 8
	v_and_b32_e32 v11, 0x2ffc, v2
	v_add_u32_e32 v88, 0x800, v2
	v_add_u32_e32 v89, 0x1000, v2
	s_cselect_b32 s11, s77, s79
	s_cselect_b32 s10, s76, s78
	s_cmpk_lt_u32 s2, 0x4000
	v_add_u32_e32 v2, 0x1800, v2
	v_lshlrev_b32_e32 v11, 2, v11
	v_and_b32_e32 v92, 0x3ffc, v88
	v_cmp_gt_u32_e32 vcc, s5, v88
	v_and_b32_e32 v93, 0x3ffc, v89
	s_cselect_b32 s13, s77, s79
	v_cndmask_b32_e32 v97, v7, v8, vcc
	s_cselect_b32 s12, s76, s78
	v_and_b32_e32 v98, 0x3ffc, v2
	v_cmp_gt_u32_e64 s[0:1], s5, v2
	global_load_dwordx4 v[88:91], v11, s[10:11]
	v_cndmask_b32_e32 v96, v9, v10, vcc
	v_lshlrev_b32_e32 v2, 2, v92
	v_lshlrev_b32_e32 v11, 2, v93
	v_cndmask_b32_e64 v101, v7, v8, s[0:1]
	v_cndmask_b32_e64 v100, v9, v10, s[0:1]
	global_load_dwordx4 v[92:95], v11, s[12:13]
	v_lshl_add_u64 v[96:97], v[96:97], 0, v[2:3]
	v_lshlrev_b32_e32 v2, 2, v98
	global_load_dwordx4 v[96:99], v[96:97], off
	v_lshl_add_u64 v[100:101], v[100:101], 0, v[2:3]
	global_load_dwordx4 v[100:103], v[100:101], off
	s_add_i32 s6, s6, 4
	s_addk_i32 s2, 0x2000
	s_cmpk_eq_u32 s2, 0x8000
	s_waitcnt vmcnt(15)
; #define GAS __attribute__((address_space(1)))
; #define LAS __attribute__((address_space(3)))
; DI unsigned pk2(float lo, float hi) { return f2bf(lo) | (f2bf(hi) << 16); }
; DI void p8_phase(Frame& F) {
;     ...
;     for (int i = 0; i < 16; ++i) { const int idx = tid * 4 + 2048 * i, side = idx >> 14, rem = idx & 16383, row = rem >> 7, col = rem & 127;
;         const f32x4 a = *(const GAS f32x4*)((side ? F.keys2 : F.keys1) + rem);
;         v2u o; o.x = pk2(a.x, a.y); o.y = pk2(a.z, a.w); *(LAS v2u*)(KIMG + (side * 128 + row) * KPITCH + col * 2) = o; }
;     __syncthreads();
;     const int gcT = F.vcu * NWAVES + F.wave, NGWT = F.G * NWAVES; int trow_it = 0;
	v_bfe_u32 v2, v40, 16, 1
	v_bfe_u32 v28, v42, 16, 1
	v_bfe_u32 v11, v41, 16, 1
	v_bfe_u32 v29, v43, 16, 1
	v_add3_u32 v2, v40, v2, s3
	v_add3_u32 v40, v42, v28, s3
	s_waitcnt vmcnt(14)
	v_bfe_u32 v42, v44, 16, 1
	v_bfe_u32 v28, v46, 16, 1
	v_add3_u32 v11, v41, v11, s3
	v_add3_u32 v41, v43, v29, s3
	v_bfe_u32 v43, v45, 16, 1
	v_bfe_u32 v29, v47, 16, 1
	v_lshrrev_b32_e32 v2, 16, v2
	v_lshrrev_b32_e32 v30, 16, v40
	s_waitcnt vmcnt(13)
	v_bfe_u32 v31, v48, 16, 1
	v_bfe_u32 v33, v50, 16, 1
	v_add3_u32 v42, v44, v42, s3
	v_add3_u32 v44, v46, v28, s3
	v_bfe_u32 v32, v49, 16, 1
	v_bfe_u32 v34, v51, 16, 1
	v_add3_u32 v43, v45, v43, s3
	v_add3_u32 v45, v47, v29, s3
	v_and_or_b32 v40, v11, s4, v2
	v_and_or_b32 v41, v41, s4, v30
	v_add3_u32 v2, v48, v31, s3
	v_add3_u32 v46, v50, v33, s3
	v_lshrrev_b32_e32 v44, 16, v44
	s_waitcnt vmcnt(12)
	v_bfe_u32 v48, v52, 16, 1
	v_bfe_u32 v50, v54, 16, 1
	v_add3_u32 v11, v49, v32, s3
	v_add3_u32 v47, v51, v34, s3
	v_lshrrev_b32_e32 v42, 16, v42
	v_bfe_u32 v49, v53, 16, 1
	v_bfe_u32 v51, v55, 16, 1
	ds_write_b64 v6, v[40:41]
	v_lshrrev_b32_e32 v2, 16, v2
	v_lshrrev_b32_e32 v46, 16, v46
	v_and_or_b32 v41, v45, s4, v44
	v_add3_u32 v44, v52, v48, s3
	v_add3_u32 v48, v54, v50, s3
	v_and_or_b32 v40, v43, s4, v42
	v_add3_u32 v45, v53, v49, s3
	v_add3_u32 v49, v55, v51, s3
	v_and_or_b32 v42, v11, s4, v2
	v_and_or_b32 v43, v47, s4, v46
	v_lshrrev_b32_e32 v2, 16, v44
	v_lshrrev_b32_e32 v11, 16, v48
	ds_write_b64 v5, v[42:43]
	ds_write_b64 v4, v[40:41]
	v_and_or_b32 v40, v45, s4, v2
	v_and_or_b32 v41, v49, s4, v11
	ds_write_b64 v1, v[40:41]
	s_waitcnt vmcnt(11)
	v_bfe_u32 v2, v56, 16, 1
	v_bfe_u32 v28, v58, 16, 1
	v_bfe_u32 v11, v57, 16, 1
	v_bfe_u32 v29, v59, 16, 1
	v_add3_u32 v2, v56, v2, s3
	v_add3_u32 v56, v58, v28, s3
	s_waitcnt vmcnt(10)
	v_bfe_u32 v58, v60, 16, 1
	v_bfe_u32 v28, v62, 16, 1
	v_add3_u32 v11, v57, v11, s3
	v_add3_u32 v57, v59, v29, s3
	v_bfe_u32 v59, v61, 16, 1
	v_bfe_u32 v29, v63, 16, 1
	v_lshrrev_b32_e32 v2, 16, v2
	v_lshrrev_b32_e32 v30, 16, v56
	s_waitcnt vmcnt(9)
	v_bfe_u32 v31, v64, 16, 1
	v_bfe_u32 v33, v66, 16, 1
	v_add3_u32 v58, v60, v58, s3
	v_add3_u32 v60, v62, v28, s3
	v_bfe_u32 v32, v65, 16, 1
	v_bfe_u32 v34, v67, 16, 1
	v_add3_u32 v59, v61, v59, s3
	v_add3_u32 v61, v63, v29, s3
	v_and_or_b32 v56, v11, s4, v2
	v_and_or_b32 v57, v57, s4, v30
	v_add3_u32 v2, v64, v31, s3
	v_add3_u32 v62, v66, v33, s3
	v_lshrrev_b32_e32 v60, 16, v60
	s_waitcnt vmcnt(8)
	v_bfe_u32 v64, v68, 16, 1
	v_bfe_u32 v66, v70, 16, 1
	v_add3_u32 v11, v65, v32, s3
	v_add3_u32 v63, v67, v34, s3
	v_lshrrev_b32_e32 v58, 16, v58
	v_bfe_u32 v65, v69, 16, 1
	v_bfe_u32 v67, v71, 16, 1
	ds_write_b64 v6, v[56:57] offset:17408
	v_lshrrev_b32_e32 v2, 16, v2
	v_lshrrev_b32_e32 v62, 16, v62
	v_and_or_b32 v57, v61, s4, v60
	v_add3_u32 v60, v68, v64, s3
	v_add3_u32 v64, v70, v66, s3
	v_and_or_b32 v56, v59, s4, v58
	v_add3_u32 v61, v69, v65, s3
	v_add3_u32 v65, v71, v67, s3
	v_and_or_b32 v58, v11, s4, v2
	v_and_or_b32 v59, v63, s4, v62
	v_lshrrev_b32_e32 v2, 16, v60
	v_lshrrev_b32_e32 v11, 16, v64
	ds_write_b64 v5, v[58:59] offset:17408
	ds_write_b64 v4, v[56:57] offset:17408
	v_and_or_b32 v56, v61, s4, v2
	v_and_or_b32 v57, v65, s4, v11
	ds_write_b64 v1, v[56:57] offset:17408
	s_waitcnt vmcnt(7)
	v_bfe_u32 v2, v72, 16, 1
	v_bfe_u32 v28, v74, 16, 1
	v_bfe_u32 v11, v73, 16, 1
	v_bfe_u32 v29, v75, 16, 1
	v_add3_u32 v2, v72, v2, s3
	v_add3_u32 v72, v74, v28, s3
	s_waitcnt vmcnt(6)
	v_bfe_u32 v74, v76, 16, 1
	v_bfe_u32 v28, v78, 16, 1
	v_add3_u32 v11, v73, v11, s3
	v_add3_u32 v73, v75, v29, s3
	v_bfe_u32 v75, v77, 16, 1
	v_bfe_u32 v29, v79, 16, 1
	v_lshrrev_b32_e32 v2, 16, v2
	v_lshrrev_b32_e32 v30, 16, v72
	s_waitcnt vmcnt(5)
	v_bfe_u32 v31, v80, 16, 1
	v_bfe_u32 v33, v82, 16, 1
	v_add3_u32 v74, v76, v74, s3
	v_add3_u32 v76, v78, v28, s3
	v_bfe_u32 v32, v81, 16, 1
	v_bfe_u32 v34, v83, 16, 1
	v_add3_u32 v75, v77, v75, s3
	v_add3_u32 v77, v79, v29, s3
	v_and_or_b32 v72, v11, s4, v2
	v_and_or_b32 v73, v73, s4, v30
	v_add3_u32 v2, v80, v31, s3
	v_add3_u32 v78, v82, v33, s3
	v_lshrrev_b32_e32 v76, 16, v76
	s_waitcnt vmcnt(4)
	v_bfe_u32 v80, v84, 16, 1
	v_bfe_u32 v82, v86, 16, 1
	v_add3_u32 v11, v81, v32, s3
	v_add3_u32 v79, v83, v34, s3
	v_lshrrev_b32_e32 v74, 16, v74
	v_bfe_u32 v81, v85, 16, 1
	v_bfe_u32 v83, v87, 16, 1
	ds_write_b64 v6, v[72:73] offset:34816
	v_lshrrev_b32_e32 v2, 16, v2
	v_lshrrev_b32_e32 v78, 16, v78
	v_and_or_b32 v73, v77, s4, v76
	v_add3_u32 v76, v84, v80, s3
	v_add3_u32 v80, v86, v82, s3
	v_and_or_b32 v72, v75, s4, v74
	v_add3_u32 v77, v85, v81, s3
	v_add3_u32 v81, v87, v83, s3
	v_and_or_b32 v74, v11, s4, v2
	v_and_or_b32 v75, v79, s4, v78
	v_lshrrev_b32_e32 v2, 16, v76
	v_lshrrev_b32_e32 v11, 16, v80
	ds_write_b64 v5, v[74:75] offset:34816
	ds_write_b64 v4, v[72:73] offset:34816
	v_and_or_b32 v72, v77, s4, v2
	v_and_or_b32 v73, v81, s4, v11
	ds_write_b64 v1, v[72:73] offset:34816
	s_waitcnt vmcnt(3)
	v_bfe_u32 v2, v88, 16, 1
	v_bfe_u32 v28, v90, 16, 1
	v_bfe_u32 v11, v89, 16, 1
	v_bfe_u32 v29, v91, 16, 1
	v_add3_u32 v2, v88, v2, s3
	v_add3_u32 v88, v90, v28, s3
	s_waitcnt vmcnt(2)
	v_bfe_u32 v90, v92, 16, 1
	v_bfe_u32 v28, v94, 16, 1
	v_add3_u32 v11, v89, v11, s3
	v_add3_u32 v89, v91, v29, s3
	v_bfe_u32 v91, v93, 16, 1
	v_bfe_u32 v29, v95, 16, 1
	v_lshrrev_b32_e32 v2, 16, v2
	v_lshrrev_b32_e32 v30, 16, v88
	s_waitcnt vmcnt(1)
	v_bfe_u32 v31, v96, 16, 1
	v_bfe_u32 v33, v98, 16, 1
	v_add3_u32 v90, v92, v90, s3
	v_add3_u32 v92, v94, v28, s3
	v_bfe_u32 v32, v97, 16, 1
	v_bfe_u32 v34, v99, 16, 1
	v_add3_u32 v91, v93, v91, s3
	v_add3_u32 v93, v95, v29, s3
	v_and_or_b32 v88, v11, s4, v2
	v_and_or_b32 v89, v89, s4, v30
	v_add3_u32 v2, v96, v31, s3
	v_add3_u32 v94, v98, v33, s3
	v_lshrrev_b32_e32 v92, 16, v92
	s_waitcnt vmcnt(0)
	v_bfe_u32 v96, v100, 16, 1
	v_bfe_u32 v98, v102, 16, 1
	v_add3_u32 v11, v97, v32, s3
	v_add3_u32 v95, v99, v34, s3
	v_lshrrev_b32_e32 v90, 16, v90
	v_bfe_u32 v97, v101, 16, 1
	v_bfe_u32 v99, v103, 16, 1
	ds_write_b64 v6, v[88:89] offset:52224
	v_lshrrev_b32_e32 v2, 16, v2
	v_lshrrev_b32_e32 v94, 16, v94
	v_and_or_b32 v89, v93, s4, v92
	v_add3_u32 v92, v100, v96, s3
	v_add3_u32 v96, v102, v98, s3
	v_and_or_b32 v88, v91, s4, v90
	v_add3_u32 v93, v101, v97, s3
	v_add3_u32 v97, v103, v99, s3
	v_and_or_b32 v90, v11, s4, v2
	v_and_or_b32 v91, v95, s4, v94
	v_lshrrev_b32_e32 v2, 16, v92
	v_lshrrev_b32_e32 v11, 16, v96
	ds_write_b64 v5, v[90:91] offset:52224
	ds_write_b64 v4, v[88:89] offset:52224
	v_and_or_b32 v88, v93, s4, v2
	v_and_or_b32 v89, v97, s4, v11
	ds_write_b64 v1, v[88:89] offset:52224
	v_add_u32_e32 v6, 0x11000, v6
	v_add_u32_e32 v4, 0x11000, v4
	v_add_u32_e32 v5, 0x11000, v5
	v_add_u32_e32 v1, 0x11000, v1
	v_readlane_b32 s0, v252, 12
	s_lshl_b32 s35, s0, 3
	v_readlane_b32 s0, v252, 11
	s_lshl_b32 s34, s0, 3
	s_andn2_b64 vcc, exec, s[22:23]
	s_mov_b32 s10, 0
	s_waitcnt lgkmcnt(0)
	s_barrier
; #define GAS __attribute__((address_space(1)))
; #define LAS __attribute__((address_space(3)))
; DI unsigned pk2(float lo, float hi) { return f2bf(lo) | (f2bf(hi) << 16); }
; DI int crow(int reg, int h) { return (reg & 3) + 8 * (reg >> 2) + 4 * h; }
; DI void p8_phase(Frame& F) {
;     LAS unsigned char* KIMG = F.lds; LAS unsigned char* TBL = F.lds + P8_TBL + F.wave * 1024;
;     const int lane = F.lane, tid = F.tid, r = lane & 31, h = lane >> 5;
; #pragma unroll 4
;     for (int i = 0; i < 16; ++i) { const int idx = tid * 4 + 2048 * i, side = idx >> 14, rem = idx & 16383, row = rem >> 7, col = rem & 127;
;         const f32x4 a = *(const GAS f32x4*)((side ? F.keys2 : F.keys1) + rem);
;         v2u o; o.x = pk2(a.x, a.y); o.y = pk2(a.z, a.w); *(LAS v2u*)(KIMG + (side * 128 + row) * KPITCH + col * 2) = o; }
;     __syncthreads();
;     const int gcT = F.vcu * NWAVES + F.wave, NGWT = F.G * NWAVES; int trow_it = 0;
;     for (int it = (int)blockIdx.x; it < (M / 256) * PH; it += F.G, ++trow_it) {
;         const int tile = it / PH, hd = it % PH;
;         const int t = tile * 256 + F.wave * 32 + r;
;     ...
;                 for (int reg = 0; reg < 16; ++reg) { const unsigned key = (unsigned)(kt * 32 + crow(reg, h)); const float sv = acc[kt][reg];
;                     topk_insert(L, __uint_as_float((__float_as_uint(sv) & ~127u) | key)); }
	s_cbranch_vccnz .LBB0_1237
	v_mbcnt_hi_u32_b32 v1, -1, v200
	v_and_b32_e32 v3, 64, v1
	v_xor_b32_e32 v2, 32, v1
	v_add_u32_e32 v3, 64, v3
	s_lshl_b32 s0, s89, 10
	v_cmp_lt_i32_e32 vcc, v2, v3
	s_add_i32 s0, s0, 0
	s_add_i32 s2, s0, 0x11000
	v_cndmask_b32_e32 v1, v1, v2, vcc
	v_lshlrev_b32_e32 v130, 3, v197
	v_lshlrev_b32_e32 v131, 2, v197
	v_lshlrev_b32_e32 v137, 2, v1
	v_lshlrev_b32_e32 v1, 5, v148
	s_add_i32 s36, s35, s89
	s_mov_b32 s11, 0
	v_mov_b32_e32 v133, 0
	v_cmp_gt_u32_e64 s[0:1], 32, v148
	v_cmp_lt_u32_e64 s[6:7], 31, v148
	v_lshl_add_u32 v139, v149, 5, s2
	v_lshl_add_u32 v144, v197, 4, 0
	v_lshl_or_b32 v145, s89, 5, v149
	v_cmp_eq_u32_e64 s[4:5], 0, v148
	v_or_b32_e32 v147, 1, v131
	v_or_b32_e32 v151, 2, v131
	v_or_b32_e32 v152, 3, v131
	v_or_b32_e32 v153, 8, v131
	v_or_b32_e32 v154, 9, v131
	v_or_b32_e32 v155, 10, v131
	v_or_b32_e32 v156, 11, v131
	v_or_b32_e32 v157, 16, v131
	v_or_b32_e32 v158, 17, v131
	v_or_b32_e32 v159, 18, v131
	v_or_b32_e32 v160, 19, v131
	v_or_b32_e32 v161, 24, v131
	v_or_b32_e32 v162, 25, v131
	v_or_b32_e32 v163, 26, v131
	v_or_b32_e32 v164, 27, v131
	v_or_b32_e32 v165, 32, v131
	v_or_b32_e32 v166, 33, v131
	v_or_b32_e32 v167, 34, v131
	v_or_b32_e32 v168, 35, v131
	v_or_b32_e32 v169, 40, v131
	v_or_b32_e32 v170, 41, v131
	v_or_b32_e32 v171, 42, v131
	v_or_b32_e32 v172, 43, v131
	v_or_b32_e32 v173, 48, v131
	v_or_b32_e32 v174, 49, v131
	v_or_b32_e32 v175, 50, v131
	v_or_b32_e32 v176, 51, v131
	v_or_b32_e32 v177, 56, v131
	v_or_b32_e32 v178, 57, v131
	v_or_b32_e32 v179, 58, v131
	v_or_b32_e32 v180, 59, v131
	v_or_b32_e32 v181, 64, v131
	v_or_b32_e32 v182, 0x41, v131
	v_or_b32_e32 v183, 0x42, v131
	v_or_b32_e32 v184, 0x43, v131
	v_or_b32_e32 v185, 0x48, v131
	v_or_b32_e32 v186, 0x49, v131
	v_or_b32_e32 v187, 0x4a, v131
	v_or_b32_e32 v188, 0x4b, v131
	v_or_b32_e32 v189, 0x50, v131
	v_or_b32_e32 v190, 0x51, v131
	v_or_b32_e32 v191, 0x52, v131
	v_or_b32_e32 v192, 0x53, v131
	v_or_b32_e32 v193, 0x58, v131
	v_or_b32_e32 v194, 0x59, v131
	v_or_b32_e32 v195, 0x5a, v131
	v_or_b32_e32 v196, 0x5b, v131
	v_or_b32_e32 v198, 0x60, v131
	v_or_b32_e32 v199, 0x61, v131
	v_or_b32_e32 v201, 0x62, v131
	v_or_b32_e32 v202, 0x63, v131
	v_or_b32_e32 v203, 0x68, v131
	v_or_b32_e32 v204, 0x69, v131
	v_or_b32_e32 v205, 0x6a, v131
	v_or_b32_e32 v206, 0x6b, v131
	v_or_b32_e32 v207, 0x70, v131
	v_or_b32_e32 v208, 0x71, v131
	v_or_b32_e32 v209, 0x72, v131
	v_or_b32_e32 v210, 0x73, v131
	v_or_b32_e32 v211, 0x78, v131
	v_or_b32_e32 v212, 0x79, v131
	v_or_b32_e32 v213, 0x7a, v131
	v_or_b32_e32 v214, 0x7b, v131
	s_movk_i32 s38, 0xff00
	v_lshlrev_b32_e32 v134, 1, v130
	s_movk_i32 s40, 0x110
	s_movk_i32 s41, 0x1000
	s_mov_b32 s42, 0x42fe0000
	s_mov_b32 s43, 0x40c0c00
	s_movk_i32 s44, 0xff80
	s_mov_b32 s45, 0xff61b1e6
	v_add_u32_e32 v215, s2, v1
	s_mov_b32 s46, 0
	s_mov_b32 s47, s58
	s_bitcmp1_b32 s89, 2
	s_cbranch_scc0 .Lp7_noskew
	s_sleep 127
.Lp7_noskew:
	s_branch .LBB0_1207
